# layer-1 expert weight copies of the combine phase moved to the idle waves 2..7 of the layer-1 router phase
# speedup vs baseline: 1.0067x; 1.0067x over previous
; #define LAS __attribute__((address_space(3)))
; template <class T> __device__ __forceinline__ T* wsp(const Frame& F, size_t off) { return (T*)(F.ws + off); }
; #define REPS(k) for (int rep_ = 0; rep_ <= (int)((REPEAT_MASK >> (k)) & 1u); ++rep_)
; #define SEAM(k) do { if (lo <= (k) && (k) + 1 < hi) xcd_barrier(bar); } while (0)
;     LAS float* scr = (LAS float*)(F.lds + RING_OFF + F.wave * 16384);
;     const int gw = (ncu ? (int)blockIdx.x - cu0 : F.vcu) * NWAVES + F.wave, NGW = (ncu ? ncu : F.G) * NWAVES;
;     bf16* UP = wsp<bf16>(F, WS_WEUP); bf16* DN = wsp<bf16>(F, WS_WEDN);
;     for (int it = it0 + gw; it < it1; it += NGW) {
;         const int e = it / 384, r = it % 384; const size_t eo = (size_t)(layer * 64 + e) * 1024 * 256;
;         if (r < 128) p0_transpose_item(inp(F, I_WGATE) + eo, 1024, 256, UP + (size_t)e * 512 * 1024, 3, scr, r, F.lane);
;         else if (r < 256) p0_transpose_item(inp(F, I_WUP) + eo, 1024, 256, UP + (size_t)e * 512 * 1024, 4, scr, r - 128, F.lane);
;         else p0_transpose_item(inp(F, I_WDOWN) + eo, 256, 1024, DN + (size_t)e * 1024 * 256, 5, scr, r - 256, F.lane, 16.f);
;     }
; __global__ void __launch_bounds__(NWAVES * 64, 2) mega_fwd(Args args) {
;     ...
;     if (IN(PH_CMB)) REPS(PH_CMB) { FENCE(F); phase_combine(F); FENCE(F); convert_experts(F, 1, (CVT_EARLY > 0 && F.G == 256) ? CVT_EARLY : 0); } SEAM(PH_CMB);
.LBB0_1304:
	s_cmpk_eq_i32 s67, 0x100
	s_cbranch_scc1 .LBB0_1315
	s_cmpk_eq_i32 s67, 0x100
	v_mov_b32_e32 v2, v0
	s_cselect_b32 s4, 0x2000, 0
	s_add_i32 s4, s9, s4
	v_readfirstlane_b32 s5, v2
	s_ashr_i32 s5, s5, 6
	s_add_i32 s5, s4, s5
	s_movk_i32 s3, 0x2000
	s_cmpk_gt_i32 s5, 0x5fff
	s_cbranch_scc1 .LBB0_1315
	s_add_u32 s9, s38, 0x4800000
	s_addc_u32 s18, s39, 0
	s_add_u32 s19, s38, 0x2800000
	v_and_b32_e32 v1, 56, v2
	v_lshlrev_b32_e32 v2, 2, v2
	s_addc_u32 s20, s39, 0
	v_and_b32_e32 v10, 28, v2
	s_lshl_b32 s21, s5, 6
	s_lshl_b32 s22, s2, 6
	s_lshl_b32 s23, s5, 5
	s_lshl_b32 s40, s2, 5
	s_lshl_b32 s41, s5, 3
	s_lshl_b32 s42, s2, 3
	s_lshl_b32 s43, s5, 1
	s_lshl_b32 s44, s2, 1
	s_add_i32 s45, 0, 0x202a8
	s_waitcnt lgkmcnt(1)
	v_mov_b32_e32 v7, 0
	s_movk_i32 s46, 0x1000
	s_movk_i32 s47, 0x4000
	s_movk_i32 s48, 0x6000
	s_movk_i32 s49, 0x7000
	s_mov_b32 s4, 0x41800000
	s_movk_i32 s50, 0x7fff
	s_mov_b32 s51, 0xffff0000
	s_mov_b64 s[10:11], 0x600
	s_add_i32 s52, 0, 0x202a0
	s_add_i32 s53, 0, 0x20298
	v_mov_b32_e32 v11, 1
	v_mov_b32_e32 v12, 0x400
	v_mov_b32_e32 v13, 0x7c
	s_branch .LBB0_1307

; #define LAS __attribute__((address_space(3)))
; template <class T> __device__ __forceinline__ T* wsp(const Frame& F, size_t off) { return (T*)(F.ws + off); }
;     LAS float* scr = (LAS float*)(F.lds + RING_OFF + F.wave * 16384);
;     const int gw = (ncu ? (int)blockIdx.x - cu0 : F.vcu) * NWAVES + F.wave, NGW = (ncu ? ncu : F.G) * NWAVES;
;     bf16* UP = wsp<bf16>(F, WS_WEUP); bf16* DN = wsp<bf16>(F, WS_WEDN);
;     for (int it = it0 + gw; it < it1; it += NGW) {
;         const int e = it / 384, r = it % 384; const size_t eo = (size_t)(layer * 64 + e) * 1024 * 256;
;         if (r < 128) p0_transpose_item(inp(F, I_WGATE) + eo, 1024, 256, UP + (size_t)e * 512 * 1024, 3, scr, r, F.lane);
;         else if (r < 256) p0_transpose_item(inp(F, I_WUP) + eo, 1024, 256, UP + (size_t)e * 512 * 1024, 4, scr, r - 128, F.lane);
;         else p0_transpose_item(inp(F, I_WDOWN) + eo, 256, 1024, DN + (size_t)e * 1024 * 256, 5, scr, r - 256, F.lane, 16.f);
;     }
.Lcv1_entry:
	s_cmpk_lg_i32 s67, 0x100
	s_cbranch_scc1 .Lcv1_end
	v_mov_b32_e32 v2, v0
	s_mul_i32 s4, s71, 6
	s_movk_i32 s2, 0x600
	v_readfirstlane_b32 s5, v2
	s_movk_i32 s3, 0x2000
	s_ashr_i32 s5, s5, 6
	s_add_i32 s5, s5, s4
	s_addk_i32 s5, 0x1ffe
	s_cmpk_gt_i32 s5, 0x5fff
	s_cbranch_scc1 .Lcv1_end
	s_add_u32 s9, s38, 0x4800000
	s_addc_u32 s18, s39, 0
	s_add_u32 s19, s38, 0x2800000
	v_and_b32_e32 v1, 56, v2
	v_lshlrev_b32_e32 v2, 2, v2
	s_addc_u32 s20, s39, 0
	v_and_b32_e32 v10, 28, v2
	s_lshl_b32 s21, s5, 6
	s_lshl_b32 s22, s2, 6
	s_lshl_b32 s23, s5, 5
	s_lshl_b32 s40, s2, 5
	s_lshl_b32 s41, s5, 3
	s_lshl_b32 s42, s2, 3
	s_lshl_b32 s43, s5, 1
	s_lshl_b32 s44, s2, 1
	s_add_i32 s45, 0, 0x202a8
	s_waitcnt lgkmcnt(1)
	v_mov_b32_e32 v7, 0
	s_movk_i32 s46, 0x1000
	s_movk_i32 s47, 0x4000
	s_movk_i32 s48, 0x6000
	s_movk_i32 s49, 0x7000
	s_mov_b32 s4, 0x41800000
	s_movk_i32 s50, 0x7fff
	s_mov_b32 s51, 0xffff0000
	s_mov_b64 s[10:11], 0x600
	s_add_i32 s52, 0, 0x202a0
	s_add_i32 s53, 0, 0x20298
	v_mov_b32_e32 v11, 1
	v_mov_b32_e32 v12, 0x400
	v_mov_b32_e32 v13, 0x7c
	s_branch .Lcv1_07

;     __device__ __forceinline__ void st(const void* p, const u32x4& v) const { __builtin_amdgcn_raw_buffer_store_b128(v, r, (unsigned)((const unsigned char*)p - b), 0, EPI_SC1); }
; __device__ __forceinline__ unsigned xb_ld(unsigned* p)              { return __hip_atomic_load(p, __ATOMIC_RELAXED, __HIP_MEMORY_SCOPE_AGENT); }
; __device__ __forceinline__ void xcd_barrier_complete(unsigned* bar, unsigned x, unsigned& nloc, unsigned& nx) {
;     const unsigned G = gridDim.x * gridDim.y * gridDim.z;
;     unsigned sum, cnt, mine, sp = 0u;
;     for (;;) {
;         sum = 0u; cnt = 0u; mine = 0u;
; #pragma unroll
;         for (unsigned j = 0; j < 16; ++j) { const unsigned c = xb_ld(&bar[XB_XCNT(j)]); sum += c; cnt += (c > 0u) ? 1u : 0u; mine = (j == x) ? c : mine; }
;         if (sum == G) break;
;         __builtin_amdgcn_s_sleep(1);
;         if ((++sp & 255u) == 0u) { if (xb_ld(&bar[XB_TMO])) break; if (sp > XB_SPIN_CAP) { atomicAdd(&bar[XB_TMO], 1u); break; } }
;     }
;     nloc = mine > 0u ? mine : 1u; nx = cnt > 0u ? cnt : 1u;
; }
; __device__ __forceinline__ void xcd_barrier(const XcdBarrier& b) {
;     asm volatile("s_waitcnt vmcnt(0)" ::: "memory");
;     __syncthreads();
;     if (threadIdx.x == 0) {
;         unsigned* bar = b.bar;
;         __builtin_amdgcn_s_waitcnt(0);
;         unsigned nloc = b.st[0], nx = b.st[1];
;         if (nloc == 0u) { xcd_barrier_complete(bar, b.x, nloc, nx); b.st[0] = nloc; b.st[1] = nx; }
.Lcv1_end:
.LBB0_1532:
	s_cmp_gt_i32 s35, 16
	s_cselect_b64 s[2:3], -1, 0
	s_and_b64 s[0:1], s[0:1], s[2:3]
	s_andn2_b64 vcc, exec, s[0:1]
	s_cbranch_vccnz .LBB0_1586
	s_waitcnt vmcnt(0)
	s_waitcnt vmcnt(0) lgkmcnt(0)
	s_barrier
	s_and_saveexec_b64 s[0:1], s[6:7]
	s_cbranch_execz .LBB0_1585
	s_add_i32 s4, 0, 0x20160
	v_mov_b32_e32 v1, s4
	s_waitcnt vmcnt(0) expcnt(0) lgkmcnt(0)
	ds_read_b32 v3, v1
	s_add_i32 s4, 0, 0x20164
	v_mov_b32_e32 v1, s4
	ds_read_b32 v1, v1
	s_waitcnt lgkmcnt(1)
	v_cmp_ne_u32_e32 vcc, 0, v3
	s_cbranch_vccnz .LBB0_1549
	s_load_dwordx2 s[10:11], s[92:93], 0x4
	s_add_u32 s4, s26, 0x4200
	s_addc_u32 s5, s27, 0
	s_add_u32 s8, s26, 0x4400
	s_addc_u32 s9, s27, 0
	s_waitcnt lgkmcnt(0)
	s_mul_i32 s62, s10, s67
	s_add_u32 s10, s26, 0x4500
	s_mul_i32 s62, s62, s11
	s_addc_u32 s11, s27, 0
	s_add_u32 s12, s26, 0x4600
	s_addc_u32 s13, s27, 0
	s_add_u32 s14, s26, 0x4700
	s_addc_u32 s15, s27, 0
	s_add_u32 s16, s26, 0x4800
	s_addc_u32 s17, s27, 0
	s_add_u32 s18, s26, 0x4900
	s_addc_u32 s19, s27, 0
	s_add_u32 s20, s26, 0x4a00
	s_addc_u32 s21, s27, 0
	s_add_u32 s22, s26, 0x4b00
	s_addc_u32 s23, s27, 0
	s_add_u32 s40, s26, 0x4c00
	s_addc_u32 s41, s27, 0
	s_add_u32 s42, s26, 0x4d00
	s_addc_u32 s43, s27, 0
	s_add_u32 s44, s26, 0x4e00
	s_addc_u32 s45, s27, 0
	s_add_u32 s46, s26, 0x4f00
	s_addc_u32 s47, s27, 0
	s_add_u32 s48, s26, 0x5000
	s_addc_u32 s49, s27, 0
	s_add_u32 s50, s26, 0x5100
	s_addc_u32 s51, s27, 0
	s_add_u32 s52, s26, 0x5200
	s_addc_u32 s53, s27, 0
	s_add_u32 s54, s26, 0x5300
	s_addc_u32 s55, s27, 0
	s_mov_b32 s63, 1
	v_mov_b32_e32 v17, 0
	s_branch .LBB0_1537
